# G_P1 144->128 on top of rope-in-LDS: 9 GEMM rounds on 128 workgroups, 128 converting workgroups
# speedup vs baseline: 1.0055x; 1.0055x over previous
; __global__ void __launch_bounds__(NWAVES * 64, 2) enc_fwd(Args args) {
;     ...
;     if (IN(0) && IN(1)) { xcd_barrier_arrive(bar); if (!(G == 256 && blk >= G_P1)) xcd_barrier_wait(bar); }
.LBB0_73:
	s_or_b64 exec, exec, s[4:5]
	v_readlane_b32 s0, v254, 9
	s_cmpk_eq_i32 s0, 0x100
	v_readlane_b32 s4, v254, 10
	s_cselect_b64 s[0:1], -1, 0
	s_cmpk_gt_i32 s4, 0x7f
	s_cselect_b64 s[4:5], -1, 0
	s_and_b64 s[0:1], s[4:5], s[0:1]
	s_and_b64 vcc, exec, s[0:1]
	s_cbranch_vccnz .LBB0_90
	s_mov_b64 s[4:5], exec
	v_readlane_b32 s0, v254, 49
	v_readlane_b32 s1, v254, 50
	s_and_b64 s[0:1], s[4:5], s[0:1]
	s_mov_b64 exec, s[0:1]
	s_cbranch_execz .LBB0_89
	s_add_i32 s0, 0, 0x24168
	v_mov_b32_e32 v1, s0
	v_readlane_b32 s0, v254, 0
	v_mov_b32_e32 v2, 0x7000
	v_readlane_b32 s1, v254, 1
	ds_read_b32 v1, v1
	s_add_u32 s10, s0, 0x7400
	s_addc_u32 s11, s1, 0
	s_nop 1
	global_load_dword v2, v2, s[0:1] offset:1024 sc1
	s_waitcnt vmcnt(0) lgkmcnt(0)
	v_cmp_ge_u32_e32 vcc, v2, v1
	s_cbranch_vccnz .LBB0_88
	v_readlane_b32 s0, v254, 0
	v_readlane_b32 s1, v254, 1
	s_add_u32 s8, s0, 0x4200
	s_addc_u32 s9, s1, 0
	s_mov_b32 s0, 1
	v_mov_b32_e32 v2, 0
	s_branch .LBB0_78

; #define PHASE_IDS() do { int t_ = tid_k; asm volatile("" : "+v"(t_)); tid = t_; lane = t_ & 63; } while (0)
; #define REP(k) for (int rep_ = 0; rep_ < ((((PROBE_MASK) >> (k)) & 1) ? 2 : 1); ++rep_)
; __global__ void __launch_bounds__(NWAVES * 64, 2) enc_fwd(Args args) {
;     ...
;     bf16* XR = (bf16*)(ws + WS_XR); bf16* WIN0 = (bf16*)(ws + WS_WIN0); bf16* WOUT0 = (bf16*)(ws + WS_WOUT0); bf16* WIN1 = (bf16*)(ws + WS_WIN1); bf16* WOUT1 = (bf16*)(ws + WS_WOUT1);
;     unsigned char* WGU0 = ws + WS_WGU0; unsigned char* WDN0 = ws + WS_WDN0; unsigned char* WGU1 = ws + WS_WGU1; unsigned char* WDN1 = ws + WS_WDN1; bf16* XN = (bf16*)(ws + WS_XN); unsigned char* XN8 = ws + WS_XN8;
;     float* AFF = (float*)(ws + WS_AFF); int* SEL = (int*)(ws + WS_SEL); int* IDX = (int*)(ws + WS_IDX); float* GATE = (float*)(ws + WS_GATE);
;     f32x2* ROPE = (f32x2*)(ws + WS_ROPE);
;     bf16* AQ = (bf16*)(ws + WS_AQ); bf16* AK = (bf16*)(ws + WS_AK); bf16* AV = (bf16*)(ws + WS_AV); bf16* BQ = (bf16*)(ws + WS_BQ); bf16* BK = (bf16*)(ws + WS_BK); bf16* BV = (bf16*)(ws + WS_BV);
;     bf16* CQ = (bf16*)(ws + WS_CQ); bf16* CK = (bf16*)(ws + WS_CK); bf16* CV = (bf16*)(ws + WS_CV); bf16* OB = (bf16*)(ws + WS_O);
;     unsigned char* XS = ws + WS_XS; unsigned char* ACT = ws + WS_ACT; unsigned char* YB = ws + WS_Y;
;     ...
;     if (IN(1)) REP(1) { PHASE_IDS(); if (rep_) __syncthreads();
;         const int Gg = (G == 256) ? G_P1 : G;
;         if (blk < Gg) {
;             pg8::Gemm g{XN, WIN0, NTOK, L0_IN, DM / 2}; pg8::StaticOrder S; S.init(NTOK, L0_IN, Gg, blk);
;             pg8::EpiHeads0 E{AQ, AK, AV, BQ, BK, BV, args.in[4], args.in[5], args.in[6], args.in[7], (const pg8::f32x2e*)ROPE, QSCALE, QSCALE * KAPPA};
;             pg8::gemm_phase<pg8::EpiHeads0, pg8::StaticOrder, PG8_ALIGN, PG8_SP2, true>(lds, g, S, E);
;         } else {
;             const int ncw = G - Gg, cw = ((ncw % 8) == 0 && (Gg % 8) == 0) ? (blk % 8) * (ncw / 8) + (blk - Gg) / 8 : blk - Gg;
;             const int gwl = cw * NWAVES + wave, ngwl = ncw * NWAVES;
.LBB0_90:
	v_readlane_b32 s0, v254, 12
	v_readlane_b32 s1, v254, 13
	s_cmp_lt_i32 s0, 2
	v_readlane_b32 s4, v254, 0
	s_cselect_b64 s[0:1], -1, 0
	v_readlane_b32 s5, v254, 1
	s_add_u32 s8, s4, 0x5400000
	s_addc_u32 s9, s5, 0
	v_writelane_b32 v254, s8, 61
	s_nop 1
	v_writelane_b32 v254, s9, 62
	s_add_u32 s8, s4, 0x9400000
	s_addc_u32 s9, s5, 0
	v_writelane_b32 v254, s8, 63
	s_nop 1
	v_writelane_b32 v255, s9, 0
	s_add_u32 s8, s4, 0xb400000
	s_addc_u32 s9, s5, 0
	v_writelane_b32 v255, s8, 1
	s_nop 1
	v_writelane_b32 v255, s9, 2
	s_add_u32 s8, s4, 0xf400000
	s_addc_u32 s9, s5, 0
	v_writelane_b32 v255, s8, 3
	s_nop 1
	v_writelane_b32 v255, s9, 4
	s_add_u32 s8, s4, 0x1400000
	s_addc_u32 s9, s5, 0
	v_writelane_b32 v255, s8, 5
	s_nop 1
	v_writelane_b32 v255, s9, 6
	s_add_u32 s8, s4, 0x11400000
	s_addc_u32 s9, s5, 0
	s_add_u32 s90, s4, 0x13400000
	v_writelane_b32 v255, s8, 7
	s_addc_u32 s91, s5, 0
	s_nop 0
	v_writelane_b32 v255, s9, 8
	s_add_u32 s8, s4, 0x15400000
	s_addc_u32 s9, s5, 0
	s_add_u32 s70, s4, 0x17400000
	v_writelane_b32 v255, s8, 9
	s_addc_u32 s71, s5, 0
	s_nop 0
	v_writelane_b32 v255, s9, 10
	s_add_u32 s8, s4, 0x19400000
	v_writelane_b32 v255, s8, 11
	s_addc_u32 s8, s5, 0
	s_add_u32 s4, s4, 0x19c00000
	v_writelane_b32 v255, s8, 13
	s_addc_u32 s5, s5, 0
	v_writelane_b32 v255, s4, 15
	s_and_b64 s[20:21], s[0:1], s[2:3]
	s_andn2_b64 vcc, exec, s[20:21]
	v_writelane_b32 v255, s5, 16
	s_cbranch_vccnz .LBB0_284
	v_readlane_b32 s4, v254, 9
	s_cmpk_eq_i32 s4, 0x100
	s_cselect_b64 s[2:3], -1, 0
	s_and_b64 s[0:1], s[2:3], exec
	v_readlane_b32 s1, v254, 10
	s_cselect_b32 s74, 0x80, s4
	s_ashr_i32 s75, s1, 31
	s_lshr_b32 s0, s75, 29
	s_add_i32 s35, s1, s0
	s_and_b32 s0, s35, -8
	s_sub_i32 s34, s1, s0
	s_ashr_i32 s76, s74, 31
	s_cmp_ge_i32 s1, s74
	v_mov_b32_e32 v66, v0
	s_mov_b64 s[4:5], -1
	s_cbranch_scc0 .LBB0_141
	v_readlane_b32 s0, v254, 9
	s_sub_i32 s0, s0, s74
	v_readlane_b32 s4, v254, 10
	s_lshr_b32 s1, s0, 3
	s_sub_i32 s4, s4, s74
	s_mul_i32 s1, s1, s34
	s_lshr_b32 s5, s4, 3
	s_add_i32 s1, s1, s5
	s_or_b32 s5, s0, s74
	s_and_b32 s5, s5, 7
	s_cmp_eq_u32 s5, 0
	s_cselect_b32 s1, s1, s4
	s_lshl_b32 s1, s1, 3
	v_readlane_b32 s4, v254, 59
	s_add_i32 s36, s1, s4
	s_cmpk_gt_i32 s36, 0x25df
	s_cbranch_scc1 .LBB0_123
	s_cmpk_gt_i32 s36, 0x17ff
	s_cbranch_scc0 .LBB0_97
	s_add_i32 s18, s36, 0xfffff220
	s_cmpk_gt_u32 s18, 0xfff
	s_cbranch_scc0 .LBB0_98
	v_readlane_b32 s8, v254, 2
	s_lshl_b32 s1, s18, 4
	v_readlane_b32 s9, v254, 3
	s_and_b32 s39, s36, 15
	s_and_b32 s1, s1, 0x700
	v_readlane_b32 s10, v254, 4
	v_readlane_b32 s11, v254, 5
	s_mov_b64 s[22:23], s[8:9]
	s_mov_b32 s40, 1
	s_cbranch_execz .LBB0_99
	v_readlane_b32 s24, v255, 3
	s_mov_b32 s5, 10
	s_mov_b64 s[10:11], 21
	s_movk_i32 s4, 0x400
	s_movk_i32 s37, 0x800
	s_mov_b32 s40, 2
	s_mov_b32 s19, 0x42800000
	v_readlane_b32 s25, v255, 4
	v_mov_b32_e32 v195, s19
	s_cbranch_execz .LBB0_100
	s_branch .LBB0_106
